# T10b seam fill NW7 with shorter unit start-up: unit taken before the register save, no flag check, 6 of 16 data quads in registers that are dead at every seam (10 quads saved instead of 16)
# baseline (speedup 1.0000x reference)
; __device__ __forceinline__ void moe_convert(Frame& F, int lo, int hi, int rank, int nrank) {
;     ...
;     for (int it = lo + rank; it < hi; it += nrank) {
;         int r = it; const float* W; unsigned char* WT; int N, ldt, kind, off; float f8s;
;         if (r < 14336) { const int e = r / 1792; r -= e * 1792; W = F.in[IN_WMG] + (size_t)e * 2048 * DFFE; N = DFFE; WT = F.ws + WS_WGU1 + (size_t)e * 14336 * 2048; ldt = 2048; kind = 1; off = 0; f8s = 32.f; }
;         else if ((r -= 14336) < 14336) { const int e = r / 1792; r -= e * 1792; W = F.in[IN_WMU] + (size_t)e * 2048 * DFFE; N = DFFE; WT = F.ws + WS_WGU1 + (size_t)e * 14336 * 2048; ldt = 2048; kind = 1; off = 128; f8s = 256.f; }
;         else { r -= 14336; const int e = r / 1792; r -= e * 1792; W = F.in[IN_WMD] + (size_t)e * DFFE * 2048; N = 2048; WT = F.ws + WS_WDN1 + (size_t)e * 2048 * DFFE; ldt = DFFE; kind = 0; off = 0; f8s = 64.f; }
.LBB0_298:
	s_or_b64 exec, exec, s[0:1]
	v_readfirstlane_b32 s4, v0
	s_lshr_b32 s4, s4, 6
	s_add_i32 s5, s4, -1
	s_cmp_lt_u32 s5, 7
	s_cbranch_scc0 .Lsf0_skip
	v_mov_b32_e32 v8, 0x20020
	v_mbcnt_lo_u32_b32 v2, -1, 0
	v_mbcnt_hi_u32_b32 v2, -1, v2
	v_cmp_eq_u32_e32 vcc, 0, v2
	v_readlane_b32 s6, v247, 0
	v_readlane_b32 s7, v247, 1
	s_load_dwordx2 s[10:11], s[6:7], 0xc0
	s_load_dwordx2 s[12:13], s[6:7], 0xc8
	v_readlane_b32 s33, v247, 6
	v_cndmask_b32_e64 v18, 0, 1, vcc
	s_mul_i32 s33, s33, 112
	ds_add_rtn_u32 v9, v8, v18 offset:4
	v_mov_b32_e32 v3, 0x43e00000
	s_lshl_b32 s5, s5, 14
	v_lshl_add_u32 v7, v2, 4, s5
	s_waitcnt lgkmcnt(0)
	v_readfirstlane_b32 s18, v9
	s_cmp_ge_u32 s18, 112
	s_cbranch_scc1 .Lsf0_skip
	ds_write_b128 v7, v[160:163] offset:0
	ds_write_b128 v7, v[164:167] offset:1024
	ds_write_b128 v7, v[168:171] offset:2048
	ds_write_b128 v7, v[172:175] offset:3072
	ds_write_b128 v7, v[176:179] offset:4096
	ds_write_b128 v7, v[180:183] offset:5120
	ds_write_b128 v7, v[184:187] offset:6144
	ds_write_b128 v7, v[188:191] offset:7168
	ds_write_b128 v7, v[192:195] offset:8192
	ds_write_b128 v7, v[196:199] offset:9216
	s_add_i32 s18, s18, s33
	s_and_b32 s27, s18, 1
	s_lshr_b32 s19, s18, 1
	s_add_i32 s19, s19, 0x5000
	s_cmp_lt_u32 s19, 0x7000
	s_cbranch_scc0 .Lsf0_down
	s_add_i32 s20, s19, 0xffffc800
	s_lshr_b32 s21, s20, 8
	s_mul_i32 s21, s21, 37
	s_lshr_b32 s21, s21, 8
	s_mul_i32 s28, s21, 0x700
	s_sub_i32 s20, s20, s28
	s_mul_i32 s28, s21, 0x3800000
	s_add_u32 s14, s10, s28
	s_addc_u32 s15, s11, 0
	s_mul_i32 s28, s21, 0x1c00000
	s_add_u32 s28, s28, 0x7800000
	s_add_u32 s16, s86, s28
	s_addc_u32 s17, s87, 0
	s_movk_i32 s24, 0x7000
	s_movk_i32 s25, 0x800
	s_mov_b32 s26, 0x43800000
	s_lshr_b32 s22, s20, 4
	s_mul_i32 s22, s22, 0x2493
	s_lshr_b32 s22, s22, 16
	s_mul_i32 s28, s22, 0x70
	s_sub_i32 s23, s20, s28
	s_mov_b32 s29, 1
	s_branch .Lsf0_dec

; __device__ __forceinline__ void transpose_item_f8(const float* W, int N, unsigned char* WT, int ldt, int kind, int off, int item, int lane, float scale) {
;     const int nblk = N >> 6, kb = item / nblk, nb = item - kb * nblk, k0 = 128 * kb + 16 * (lane & 7), n = 64 * nb + 4 * (lane >> 3);
;     const f32x4* src = (const f32x4*)(W + (size_t)k0 * N + n);
;     f32x4 v[2][16];
; #pragma unroll
;     for (int hh = 0; hh < 2; ++hh)
; #pragma unroll
;         for (int j = 0; j < 16; ++j) v[hh][j] = __builtin_nontemporal_load(src + (size_t)j * (N >> 2) + 8 * hh);
.Lsf0_k0:
	s_mul_i32 s30, s30, s25
	s_lshl_b32 s31, s22, 7
	s_add_i32 s30, s30, s31
	s_add_u32 s16, s16, s30
	s_addc_u32 s17, s17, 0
	v_lshrrev_b32_e32 v6, 3, v2
	v_lshlrev_b32_e32 v6, 2, v6
	v_mul_lo_u32 v6, s25, v6
	v_lshl_add_u32 v6, v4, 4, v6
	global_load_dwordx4 v[222:225], v5, s[14:15] nt
	s_add_u32 s14, s14, s24
	s_addc_u32 s15, s15, 0
	global_load_dwordx4 v[226:229], v5, s[14:15] nt
	s_add_u32 s14, s14, s24
	s_addc_u32 s15, s15, 0
	global_load_dwordx4 v[230:233], v5, s[14:15] nt
	s_add_u32 s14, s14, s24
	s_addc_u32 s15, s15, 0
	global_load_dwordx4 v[234:237], v5, s[14:15] nt
	s_add_u32 s14, s14, s24
	s_addc_u32 s15, s15, 0
	global_load_dwordx4 v[238:241], v5, s[14:15] nt
	s_add_u32 s14, s14, s24
	s_addc_u32 s15, s15, 0
	global_load_dwordx4 v[242:245], v5, s[14:15] nt
	s_add_u32 s14, s14, s24
	s_addc_u32 s15, s15, 0
	global_load_dwordx4 v[160:163], v5, s[14:15] nt
	s_add_u32 s14, s14, s24
	s_addc_u32 s15, s15, 0
	global_load_dwordx4 v[164:167], v5, s[14:15] nt
	s_add_u32 s14, s14, s24
	s_addc_u32 s15, s15, 0
	global_load_dwordx4 v[168:171], v5, s[14:15] nt
	s_add_u32 s14, s14, s24
	s_addc_u32 s15, s15, 0
	global_load_dwordx4 v[172:175], v5, s[14:15] nt
	s_add_u32 s14, s14, s24
	s_addc_u32 s15, s15, 0
	global_load_dwordx4 v[176:179], v5, s[14:15] nt
	s_add_u32 s14, s14, s24
	s_addc_u32 s15, s15, 0
	global_load_dwordx4 v[180:183], v5, s[14:15] nt
	s_add_u32 s14, s14, s24
	s_addc_u32 s15, s15, 0
	global_load_dwordx4 v[184:187], v5, s[14:15] nt
	s_add_u32 s14, s14, s24
	s_addc_u32 s15, s15, 0
	global_load_dwordx4 v[188:191], v5, s[14:15] nt
	s_add_u32 s14, s14, s24
	s_addc_u32 s15, s15, 0
	global_load_dwordx4 v[192:195], v5, s[14:15] nt
	s_add_u32 s14, s14, s24
	s_addc_u32 s15, s15, 0
	global_load_dwordx4 v[196:199], v5, s[14:15] nt
	s_mov_b32 s28, 0xc3e00000
	s_waitcnt vmcnt(0)
; __device__ __forceinline__ unsigned pk4_fp8(float a, float b, float c, float d) { int w = 0; w = __builtin_amdgcn_cvt_pk_fp8_f32(clamp448(a), clamp448(b), w, false); w = __builtin_amdgcn_cvt_pk_fp8_f32(clamp448(c), clamp448(d), w, true); return (unsigned)w; }
; __device__ __forceinline__ void transpose_item_f8(const float* W, int N, unsigned char* WT, int ldt, int kind, int off, int item, int lane, float scale) {
;     ...
;     for (int hh = 0; hh < 2; ++hh)
; #pragma unroll
;         for (int i = 0; i < 4; ++i) { v4u o; o.x = pg8::pk4_fp8(v[hh][0][i] * scale, v[hh][1][i] * scale, v[hh][2][i] * scale, v[hh][3][i] * scale); o.y = pg8::pk4_fp8(v[hh][4][i] * scale, v[hh][5][i] * scale, v[hh][6][i] * scale, v[hh][7][i] * scale);
;             o.z = pg8::pk4_fp8(v[hh][8][i] * scale, v[hh][9][i] * scale, v[hh][10][i] * scale, v[hh][11][i] * scale); o.w = pg8::pk4_fp8(v[hh][12][i] * scale, v[hh][13][i] * scale, v[hh][14][i] * scale, v[hh][15][i] * scale);
;             __builtin_nontemporal_store(o, (v4u*)(WT + (size_t)rowmap(kind, off, n + 32 * hh + i) * ldt + k0)); }
	v_mul_f32_e32 v222, s26, v222
	v_mul_f32_e32 v223, s26, v223
	v_mul_f32_e32 v224, s26, v224
	v_mul_f32_e32 v225, s26, v225
	v_mul_f32_e32 v226, s26, v226
	v_mul_f32_e32 v227, s26, v227
	v_mul_f32_e32 v228, s26, v228
	v_mul_f32_e32 v229, s26, v229
	v_mul_f32_e32 v230, s26, v230
	v_mul_f32_e32 v231, s26, v231
	v_mul_f32_e32 v232, s26, v232
	v_mul_f32_e32 v233, s26, v233
	v_mul_f32_e32 v234, s26, v234
	v_mul_f32_e32 v235, s26, v235
	v_mul_f32_e32 v236, s26, v236
	v_mul_f32_e32 v237, s26, v237
	v_mul_f32_e32 v238, s26, v238
	v_mul_f32_e32 v239, s26, v239
	v_mul_f32_e32 v240, s26, v240
	v_mul_f32_e32 v241, s26, v241
	v_mul_f32_e32 v242, s26, v242
	v_mul_f32_e32 v243, s26, v243
	v_mul_f32_e32 v244, s26, v244
	v_mul_f32_e32 v245, s26, v245
	v_mul_f32_e32 v160, s26, v160
	v_mul_f32_e32 v161, s26, v161
	v_mul_f32_e32 v162, s26, v162
	v_mul_f32_e32 v163, s26, v163
	v_mul_f32_e32 v164, s26, v164
	v_mul_f32_e32 v165, s26, v165
	v_mul_f32_e32 v166, s26, v166
	v_mul_f32_e32 v167, s26, v167
	v_mul_f32_e32 v168, s26, v168
	v_mul_f32_e32 v169, s26, v169
	v_mul_f32_e32 v170, s26, v170
	v_mul_f32_e32 v171, s26, v171
	v_mul_f32_e32 v172, s26, v172
	v_mul_f32_e32 v173, s26, v173
	v_mul_f32_e32 v174, s26, v174
	v_mul_f32_e32 v175, s26, v175
	v_mul_f32_e32 v176, s26, v176
	v_mul_f32_e32 v177, s26, v177
	v_mul_f32_e32 v178, s26, v178
	v_mul_f32_e32 v179, s26, v179
	v_mul_f32_e32 v180, s26, v180
	v_mul_f32_e32 v181, s26, v181
	v_mul_f32_e32 v182, s26, v182
	v_mul_f32_e32 v183, s26, v183
	v_mul_f32_e32 v184, s26, v184
	v_mul_f32_e32 v185, s26, v185
	v_mul_f32_e32 v186, s26, v186
	v_mul_f32_e32 v187, s26, v187
	v_mul_f32_e32 v188, s26, v188
	v_mul_f32_e32 v189, s26, v189
	v_mul_f32_e32 v190, s26, v190
	v_mul_f32_e32 v191, s26, v191
	v_mul_f32_e32 v192, s26, v192
	v_mul_f32_e32 v193, s26, v193
	v_mul_f32_e32 v194, s26, v194
	v_mul_f32_e32 v195, s26, v195
	v_mul_f32_e32 v196, s26, v196
	v_mul_f32_e32 v197, s26, v197
	v_mul_f32_e32 v198, s26, v198
	v_mul_f32_e32 v199, s26, v199
	v_med3_f32 v222, v222, s28, v3
	v_med3_f32 v223, v223, s28, v3
	v_med3_f32 v224, v224, s28, v3
	v_med3_f32 v225, v225, s28, v3
	v_med3_f32 v226, v226, s28, v3
	v_med3_f32 v227, v227, s28, v3
	v_med3_f32 v228, v228, s28, v3
	v_med3_f32 v229, v229, s28, v3
	v_med3_f32 v230, v230, s28, v3
	v_med3_f32 v231, v231, s28, v3
	v_med3_f32 v232, v232, s28, v3
	v_med3_f32 v233, v233, s28, v3
	v_med3_f32 v234, v234, s28, v3
	v_med3_f32 v235, v235, s28, v3
	v_med3_f32 v236, v236, s28, v3
	v_med3_f32 v237, v237, s28, v3
	v_med3_f32 v238, v238, s28, v3
	v_med3_f32 v239, v239, s28, v3
	v_med3_f32 v240, v240, s28, v3
	v_med3_f32 v241, v241, s28, v3
	v_med3_f32 v242, v242, s28, v3
	v_med3_f32 v243, v243, s28, v3
	v_med3_f32 v244, v244, s28, v3
	v_med3_f32 v245, v245, s28, v3
	v_med3_f32 v160, v160, s28, v3
	v_med3_f32 v161, v161, s28, v3
	v_med3_f32 v162, v162, s28, v3
	v_med3_f32 v163, v163, s28, v3
	v_med3_f32 v164, v164, s28, v3
	v_med3_f32 v165, v165, s28, v3
	v_med3_f32 v166, v166, s28, v3
	v_med3_f32 v167, v167, s28, v3
	v_med3_f32 v168, v168, s28, v3
	v_med3_f32 v169, v169, s28, v3
	v_med3_f32 v170, v170, s28, v3
	v_med3_f32 v171, v171, s28, v3
	v_med3_f32 v172, v172, s28, v3
	v_med3_f32 v173, v173, s28, v3
	v_med3_f32 v174, v174, s28, v3
	v_med3_f32 v175, v175, s28, v3
	v_med3_f32 v176, v176, s28, v3
	v_med3_f32 v177, v177, s28, v3
	v_med3_f32 v178, v178, s28, v3
	v_med3_f32 v179, v179, s28, v3
	v_med3_f32 v180, v180, s28, v3
	v_med3_f32 v181, v181, s28, v3
	v_med3_f32 v182, v182, s28, v3
	v_med3_f32 v183, v183, s28, v3
	v_med3_f32 v184, v184, s28, v3
	v_med3_f32 v185, v185, s28, v3
	v_med3_f32 v186, v186, s28, v3
	v_med3_f32 v187, v187, s28, v3
	v_med3_f32 v188, v188, s28, v3
	v_med3_f32 v189, v189, s28, v3
	v_med3_f32 v190, v190, s28, v3
	v_med3_f32 v191, v191, s28, v3
	v_med3_f32 v192, v192, s28, v3
	v_med3_f32 v193, v193, s28, v3
	v_med3_f32 v194, v194, s28, v3
	v_med3_f32 v195, v195, s28, v3
	v_med3_f32 v196, v196, s28, v3
	v_med3_f32 v197, v197, s28, v3
	v_med3_f32 v198, v198, s28, v3
	v_med3_f32 v199, v199, s28, v3
	v_mov_b32_e32 v10, 0
	v_mov_b32_e32 v11, 0
	v_mov_b32_e32 v12, 0
	v_mov_b32_e32 v13, 0
	v_cvt_pk_fp8_f32 v10, v222, v226
	v_cvt_pk_fp8_f32 v11, v238, v242
	v_cvt_pk_fp8_f32 v12, v168, v172
	v_cvt_pk_fp8_f32 v13, v184, v188
	v_cvt_pk_fp8_f32 v10, v230, v234 op_sel:[0,0,1]
	v_cvt_pk_fp8_f32 v11, v160, v164 op_sel:[0,0,1]
	v_cvt_pk_fp8_f32 v12, v176, v180 op_sel:[0,0,1]
	v_cvt_pk_fp8_f32 v13, v192, v196 op_sel:[0,0,1]
	s_nop 1
	global_store_dwordx4 v6, v[10:13], s[16:17] nt
	s_add_u32 s16, s16, s25
	s_addc_u32 s17, s17, 0
	v_mov_b32_e32 v14, 0
	v_mov_b32_e32 v15, 0
	v_mov_b32_e32 v16, 0
	v_mov_b32_e32 v17, 0
	v_cvt_pk_fp8_f32 v14, v223, v227
	v_cvt_pk_fp8_f32 v15, v239, v243
	v_cvt_pk_fp8_f32 v16, v169, v173
	v_cvt_pk_fp8_f32 v17, v185, v189
	v_cvt_pk_fp8_f32 v14, v231, v235 op_sel:[0,0,1]
	v_cvt_pk_fp8_f32 v15, v161, v165 op_sel:[0,0,1]
	v_cvt_pk_fp8_f32 v16, v177, v181 op_sel:[0,0,1]
	v_cvt_pk_fp8_f32 v17, v193, v197 op_sel:[0,0,1]
	s_nop 1
	global_store_dwordx4 v6, v[14:17], s[16:17] nt
	s_add_u32 s16, s16, s25
	s_addc_u32 s17, s17, 0
	v_mov_b32_e32 v248, 0
	v_mov_b32_e32 v249, 0
	v_mov_b32_e32 v250, 0
	v_mov_b32_e32 v251, 0
	v_cvt_pk_fp8_f32 v248, v224, v228
	v_cvt_pk_fp8_f32 v249, v240, v244
	v_cvt_pk_fp8_f32 v250, v170, v174
	v_cvt_pk_fp8_f32 v251, v186, v190
	v_cvt_pk_fp8_f32 v248, v232, v236 op_sel:[0,0,1]
	v_cvt_pk_fp8_f32 v249, v162, v166 op_sel:[0,0,1]
	v_cvt_pk_fp8_f32 v250, v178, v182 op_sel:[0,0,1]
	v_cvt_pk_fp8_f32 v251, v194, v198 op_sel:[0,0,1]
	s_nop 1
	global_store_dwordx4 v6, v[248:251], s[16:17] nt
	s_add_u32 s16, s16, s25
	s_addc_u32 s17, s17, 0
	v_mov_b32_e32 v252, 0
	v_mov_b32_e32 v253, 0
	v_mov_b32_e32 v254, 0
	v_mov_b32_e32 v255, 0
	v_cvt_pk_fp8_f32 v252, v225, v229
	v_cvt_pk_fp8_f32 v253, v241, v245
	v_cvt_pk_fp8_f32 v254, v171, v175
	v_cvt_pk_fp8_f32 v255, v187, v191
	v_cvt_pk_fp8_f32 v252, v233, v237 op_sel:[0,0,1]
	v_cvt_pk_fp8_f32 v253, v163, v167 op_sel:[0,0,1]
	v_cvt_pk_fp8_f32 v254, v179, v183 op_sel:[0,0,1]
	v_cvt_pk_fp8_f32 v255, v195, v199 op_sel:[0,0,1]
	s_nop 1
	global_store_dwordx4 v6, v[252:255], s[16:17] nt
	ds_read_b128 v[160:163], v7 offset:0
	ds_read_b128 v[164:167], v7 offset:1024
	ds_read_b128 v[168:171], v7 offset:2048
	ds_read_b128 v[172:175], v7 offset:3072
	ds_read_b128 v[176:179], v7 offset:4096
	ds_read_b128 v[180:183], v7 offset:5120
	ds_read_b128 v[184:187], v7 offset:6144
	ds_read_b128 v[188:191], v7 offset:7168
	ds_read_b128 v[192:195], v7 offset:8192
	ds_read_b128 v[196:199], v7 offset:9216

; __device__ __forceinline__ void moe_convert(Frame& F, int lo, int hi, int rank, int nrank) {
;     ...
;     for (int it = lo + rank; it < hi; it += nrank) {
;         int r = it; const float* W; unsigned char* WT; int N, ldt, kind, off; float f8s;
;         if (r < 14336) { const int e = r / 1792; r -= e * 1792; W = F.in[IN_WMG] + (size_t)e * 2048 * DFFE; N = DFFE; WT = F.ws + WS_WGU1 + (size_t)e * 14336 * 2048; ldt = 2048; kind = 1; off = 0; f8s = 32.f; }
;         else if ((r -= 14336) < 14336) { const int e = r / 1792; r -= e * 1792; W = F.in[IN_WMU] + (size_t)e * 2048 * DFFE; N = DFFE; WT = F.ws + WS_WGU1 + (size_t)e * 14336 * 2048; ldt = 2048; kind = 1; off = 128; f8s = 256.f; }
;         else { r -= 14336; const int e = r / 1792; r -= e * 1792; W = F.in[IN_WMD] + (size_t)e * DFFE * 2048; N = 2048; WT = F.ws + WS_WDN1 + (size_t)e * 2048 * DFFE; ldt = DFFE; kind = 0; off = 0; f8s = 64.f; }
.LBB0_575:
	s_or_b64 exec, exec, s[2:3]
	v_readfirstlane_b32 s4, v0
	s_lshr_b32 s4, s4, 6
	s_add_i32 s5, s4, -1
	s_cmp_lt_u32 s5, 7
	s_cbranch_scc0 .Lsf3_skip
	v_mov_b32_e32 v8, 0x20020
	v_mbcnt_lo_u32_b32 v2, -1, 0
	v_mbcnt_hi_u32_b32 v2, -1, v2
	v_cmp_eq_u32_e32 vcc, 0, v2
	v_readlane_b32 s6, v247, 0
	v_readlane_b32 s7, v247, 1
	s_load_dwordx2 s[10:11], s[6:7], 0xc0
	s_load_dwordx2 s[12:13], s[6:7], 0xc8
	v_readlane_b32 s33, v247, 6
	v_cndmask_b32_e64 v18, 0, 1, vcc
	s_mul_i32 s33, s33, 112
	ds_add_rtn_u32 v9, v8, v18 offset:4
	v_mov_b32_e32 v3, 0x43e00000
	s_lshl_b32 s5, s5, 14
	v_lshl_add_u32 v7, v2, 4, s5
	s_waitcnt lgkmcnt(0)
	v_readfirstlane_b32 s18, v9
	s_cmp_ge_u32 s18, 112
	s_cbranch_scc1 .Lsf3_skip
	ds_write_b128 v7, v[160:163] offset:0
	ds_write_b128 v7, v[164:167] offset:1024
	ds_write_b128 v7, v[168:171] offset:2048
	ds_write_b128 v7, v[172:175] offset:3072
	ds_write_b128 v7, v[176:179] offset:4096
	ds_write_b128 v7, v[180:183] offset:5120
	ds_write_b128 v7, v[184:187] offset:6144
	ds_write_b128 v7, v[188:191] offset:7168
	ds_write_b128 v7, v[192:195] offset:8192
	ds_write_b128 v7, v[196:199] offset:9216
	s_add_i32 s18, s18, s33
	s_and_b32 s27, s18, 1
	s_lshr_b32 s19, s18, 1
	s_add_i32 s19, s19, 0x5000
	s_cmp_lt_u32 s19, 0x7000
	s_cbranch_scc0 .Lsf3_down
	s_add_i32 s20, s19, 0xffffc800
	s_lshr_b32 s21, s20, 8
	s_mul_i32 s21, s21, 37
	s_lshr_b32 s21, s21, 8
	s_mul_i32 s28, s21, 0x700
	s_sub_i32 s20, s20, s28
	s_mul_i32 s28, s21, 0x3800000
	s_add_u32 s14, s10, s28
	s_addc_u32 s15, s11, 0
	s_mul_i32 s28, s21, 0x1c00000
	s_add_u32 s28, s28, 0x7800000
	s_add_u32 s16, s86, s28
	s_addc_u32 s17, s87, 0
	s_movk_i32 s24, 0x7000
	s_movk_i32 s25, 0x800
	s_mov_b32 s26, 0x43800000
	s_lshr_b32 s22, s20, 4
	s_mul_i32 s22, s22, 0x2493
	s_lshr_b32 s22, s22, 16
	s_mul_i32 s28, s22, 0x70
	s_sub_i32 s23, s20, s28
	s_mov_b32 s29, 1
	s_branch .Lsf3_dec

; __device__ __forceinline__ void moe_convert(Frame& F, int lo, int hi, int rank, int nrank) {
;     if (MOE_DMA) { moe_convert_dma(F, lo, hi, rank, nrank); return; }
;     for (int it = lo + rank; it < hi; it += nrank) {
;         int r = it; const float* W; unsigned char* WT; int N, ldt, kind, off; float f8s;
;         if (r < 14336) { const int e = r / 1792; r -= e * 1792; W = F.in[IN_WMG] + (size_t)e * 2048 * DFFE; N = DFFE; WT = F.ws + WS_WGU1 + (size_t)e * 14336 * 2048; ldt = 2048; kind = 1; off = 0; f8s = 32.f; }
;         else if ((r -= 14336) < 14336) { const int e = r / 1792; r -= e * 1792; W = F.in[IN_WMU] + (size_t)e * 2048 * DFFE; N = DFFE; WT = F.ws + WS_WGU1 + (size_t)e * 14336 * 2048; ldt = 2048; kind = 1; off = 128; f8s = 256.f; }
;         else { r -= 14336; const int e = r / 1792; r -= e * 1792; W = F.in[IN_WMD] + (size_t)e * DFFE * 2048; N = 2048; WT = F.ws + WS_WDN1 + (size_t)e * 2048 * DFFE; ldt = DFFE; kind = 0; off = 0; f8s = 64.f; }
;         transpose_item_f8(W, N, WT, ldt, kind, off, r, F.lane, f8s);
.Lsf14_go:
	s_add_i32 s5, s4, -1
	s_lshl_b32 s5, s5, 14
	v_lshl_add_u32 v7, v2, 4, s5
	ds_write_b128 v7, v[160:163] offset:0
	ds_write_b128 v7, v[164:167] offset:1024
	ds_write_b128 v7, v[168:171] offset:2048
	ds_write_b128 v7, v[172:175] offset:3072
	ds_write_b128 v7, v[176:179] offset:4096
	ds_write_b128 v7, v[180:183] offset:5120
	ds_write_b128 v7, v[184:187] offset:6144
	ds_write_b128 v7, v[188:191] offset:7168
	ds_write_b128 v7, v[192:195] offset:8192
	ds_write_b128 v7, v[196:199] offset:9216
	v_readlane_b32 s6, v247, 0
	v_readlane_b32 s7, v247, 1
	s_load_dwordx2 s[10:11], s[6:7], 0xc0
	s_load_dwordx2 s[12:13], s[6:7], 0xc8
	v_readlane_b32 s33, v247, 6
	v_mov_b32_e32 v3, 0x43e00000
	v_cmp_eq_u32_e32 vcc, 0, v2
	s_mul_i32 s33, s33, 112
	s_nop 1
	v_cndmask_b32_e64 v18, 0, 1, vcc
	s_waitcnt lgkmcnt(0)

; __device__ __forceinline__ void transpose_item_f8(const float* W, int N, unsigned char* WT, int ldt, int kind, int off, int item, int lane, float scale) {
;     const int nblk = N >> 6, kb = item / nblk, nb = item - kb * nblk, k0 = 128 * kb + 16 * (lane & 7), n = 64 * nb + 4 * (lane >> 3);
;     const f32x4* src = (const f32x4*)(W + (size_t)k0 * N + n);
;     f32x4 v[2][16];
; #pragma unroll
;     for (int hh = 0; hh < 2; ++hh)
; #pragma unroll
;         for (int j = 0; j < 16; ++j) v[hh][j] = __builtin_nontemporal_load(src + (size_t)j * (N >> 2) + 8 * hh);
.Lsf14_k0:
	s_mul_i32 s30, s30, s25
	s_lshl_b32 s31, s22, 7
	s_add_i32 s30, s30, s31
	s_add_u32 s16, s16, s30
	s_addc_u32 s17, s17, 0
	v_lshrrev_b32_e32 v6, 3, v2
	v_lshlrev_b32_e32 v6, 2, v6
	v_mul_lo_u32 v6, s25, v6
	v_lshl_add_u32 v6, v4, 4, v6
	global_load_dwordx4 v[222:225], v5, s[14:15] nt
	s_add_u32 s14, s14, s24
	s_addc_u32 s15, s15, 0
	global_load_dwordx4 v[226:229], v5, s[14:15] nt
	s_add_u32 s14, s14, s24
	s_addc_u32 s15, s15, 0
	global_load_dwordx4 v[230:233], v5, s[14:15] nt
	s_add_u32 s14, s14, s24
	s_addc_u32 s15, s15, 0
	global_load_dwordx4 v[234:237], v5, s[14:15] nt
	s_add_u32 s14, s14, s24
	s_addc_u32 s15, s15, 0
	global_load_dwordx4 v[238:241], v5, s[14:15] nt
	s_add_u32 s14, s14, s24
	s_addc_u32 s15, s15, 0
	global_load_dwordx4 v[242:245], v5, s[14:15] nt
	s_add_u32 s14, s14, s24
	s_addc_u32 s15, s15, 0
	global_load_dwordx4 v[160:163], v5, s[14:15] nt
	s_add_u32 s14, s14, s24
	s_addc_u32 s15, s15, 0
	global_load_dwordx4 v[164:167], v5, s[14:15] nt
	s_add_u32 s14, s14, s24
	s_addc_u32 s15, s15, 0
	global_load_dwordx4 v[168:171], v5, s[14:15] nt
	s_add_u32 s14, s14, s24
	s_addc_u32 s15, s15, 0
	global_load_dwordx4 v[172:175], v5, s[14:15] nt
	s_add_u32 s14, s14, s24
	s_addc_u32 s15, s15, 0
	global_load_dwordx4 v[176:179], v5, s[14:15] nt
	s_add_u32 s14, s14, s24
	s_addc_u32 s15, s15, 0
	global_load_dwordx4 v[180:183], v5, s[14:15] nt
	s_add_u32 s14, s14, s24
	s_addc_u32 s15, s15, 0
	global_load_dwordx4 v[184:187], v5, s[14:15] nt
	s_add_u32 s14, s14, s24
	s_addc_u32 s15, s15, 0
	global_load_dwordx4 v[188:191], v5, s[14:15] nt
	s_add_u32 s14, s14, s24
	s_addc_u32 s15, s15, 0
	global_load_dwordx4 v[192:195], v5, s[14:15] nt
	s_add_u32 s14, s14, s24
	s_addc_u32 s15, s15, 0
	global_load_dwordx4 v[196:199], v5, s[14:15] nt
	s_mov_b32 s28, 0xc3e00000
	s_waitcnt vmcnt(0)
; __device__ __forceinline__ unsigned pk4_fp8(float a, float b, float c, float d) { int w = 0; w = __builtin_amdgcn_cvt_pk_fp8_f32(clamp448(a), clamp448(b), w, false); w = __builtin_amdgcn_cvt_pk_fp8_f32(clamp448(c), clamp448(d), w, true); return (unsigned)w; }
; __device__ __forceinline__ void transpose_item_f8(const float* W, int N, unsigned char* WT, int ldt, int kind, int off, int item, int lane, float scale) {
;     ...
;     for (int hh = 0; hh < 2; ++hh)
; #pragma unroll
;         for (int i = 0; i < 4; ++i) { v4u o; o.x = pg8::pk4_fp8(v[hh][0][i] * scale, v[hh][1][i] * scale, v[hh][2][i] * scale, v[hh][3][i] * scale); o.y = pg8::pk4_fp8(v[hh][4][i] * scale, v[hh][5][i] * scale, v[hh][6][i] * scale, v[hh][7][i] * scale);
;             o.z = pg8::pk4_fp8(v[hh][8][i] * scale, v[hh][9][i] * scale, v[hh][10][i] * scale, v[hh][11][i] * scale); o.w = pg8::pk4_fp8(v[hh][12][i] * scale, v[hh][13][i] * scale, v[hh][14][i] * scale, v[hh][15][i] * scale);
;             __builtin_nontemporal_store(o, (v4u*)(WT + (size_t)rowmap(kind, off, n + 32 * hh + i) * ldt + k0)); }
	v_mul_f32_e32 v222, s26, v222
	v_mul_f32_e32 v223, s26, v223
	v_mul_f32_e32 v224, s26, v224
	v_mul_f32_e32 v225, s26, v225
	v_mul_f32_e32 v226, s26, v226
	v_mul_f32_e32 v227, s26, v227
	v_mul_f32_e32 v228, s26, v228
	v_mul_f32_e32 v229, s26, v229
	v_mul_f32_e32 v230, s26, v230
	v_mul_f32_e32 v231, s26, v231
	v_mul_f32_e32 v232, s26, v232
	v_mul_f32_e32 v233, s26, v233
	v_mul_f32_e32 v234, s26, v234
	v_mul_f32_e32 v235, s26, v235
	v_mul_f32_e32 v236, s26, v236
	v_mul_f32_e32 v237, s26, v237
	v_mul_f32_e32 v238, s26, v238
	v_mul_f32_e32 v239, s26, v239
	v_mul_f32_e32 v240, s26, v240
	v_mul_f32_e32 v241, s26, v241
	v_mul_f32_e32 v242, s26, v242
	v_mul_f32_e32 v243, s26, v243
	v_mul_f32_e32 v244, s26, v244
	v_mul_f32_e32 v245, s26, v245
	v_mul_f32_e32 v160, s26, v160
	v_mul_f32_e32 v161, s26, v161
	v_mul_f32_e32 v162, s26, v162
	v_mul_f32_e32 v163, s26, v163
	v_mul_f32_e32 v164, s26, v164
	v_mul_f32_e32 v165, s26, v165
	v_mul_f32_e32 v166, s26, v166
	v_mul_f32_e32 v167, s26, v167
	v_mul_f32_e32 v168, s26, v168
	v_mul_f32_e32 v169, s26, v169
	v_mul_f32_e32 v170, s26, v170
	v_mul_f32_e32 v171, s26, v171
	v_mul_f32_e32 v172, s26, v172
	v_mul_f32_e32 v173, s26, v173
	v_mul_f32_e32 v174, s26, v174
	v_mul_f32_e32 v175, s26, v175
	v_mul_f32_e32 v176, s26, v176
	v_mul_f32_e32 v177, s26, v177
	v_mul_f32_e32 v178, s26, v178
	v_mul_f32_e32 v179, s26, v179
	v_mul_f32_e32 v180, s26, v180
	v_mul_f32_e32 v181, s26, v181
	v_mul_f32_e32 v182, s26, v182
	v_mul_f32_e32 v183, s26, v183
	v_mul_f32_e32 v184, s26, v184
	v_mul_f32_e32 v185, s26, v185
	v_mul_f32_e32 v186, s26, v186
	v_mul_f32_e32 v187, s26, v187
	v_mul_f32_e32 v188, s26, v188
	v_mul_f32_e32 v189, s26, v189
	v_mul_f32_e32 v190, s26, v190
	v_mul_f32_e32 v191, s26, v191
	v_mul_f32_e32 v192, s26, v192
	v_mul_f32_e32 v193, s26, v193
	v_mul_f32_e32 v194, s26, v194
	v_mul_f32_e32 v195, s26, v195
	v_mul_f32_e32 v196, s26, v196
	v_mul_f32_e32 v197, s26, v197
	v_mul_f32_e32 v198, s26, v198
	v_mul_f32_e32 v199, s26, v199
	v_med3_f32 v222, v222, s28, v3
	v_med3_f32 v223, v223, s28, v3
	v_med3_f32 v224, v224, s28, v3
	v_med3_f32 v225, v225, s28, v3
	v_med3_f32 v226, v226, s28, v3
	v_med3_f32 v227, v227, s28, v3
	v_med3_f32 v228, v228, s28, v3
	v_med3_f32 v229, v229, s28, v3
	v_med3_f32 v230, v230, s28, v3
	v_med3_f32 v231, v231, s28, v3
	v_med3_f32 v232, v232, s28, v3
	v_med3_f32 v233, v233, s28, v3
	v_med3_f32 v234, v234, s28, v3
	v_med3_f32 v235, v235, s28, v3
	v_med3_f32 v236, v236, s28, v3
	v_med3_f32 v237, v237, s28, v3
	v_med3_f32 v238, v238, s28, v3
	v_med3_f32 v239, v239, s28, v3
	v_med3_f32 v240, v240, s28, v3
	v_med3_f32 v241, v241, s28, v3
	v_med3_f32 v242, v242, s28, v3
	v_med3_f32 v243, v243, s28, v3
	v_med3_f32 v244, v244, s28, v3
	v_med3_f32 v245, v245, s28, v3
	v_med3_f32 v160, v160, s28, v3
	v_med3_f32 v161, v161, s28, v3
	v_med3_f32 v162, v162, s28, v3
	v_med3_f32 v163, v163, s28, v3
	v_med3_f32 v164, v164, s28, v3
	v_med3_f32 v165, v165, s28, v3
	v_med3_f32 v166, v166, s28, v3
	v_med3_f32 v167, v167, s28, v3
	v_med3_f32 v168, v168, s28, v3
	v_med3_f32 v169, v169, s28, v3
	v_med3_f32 v170, v170, s28, v3
	v_med3_f32 v171, v171, s28, v3
	v_med3_f32 v172, v172, s28, v3
	v_med3_f32 v173, v173, s28, v3
	v_med3_f32 v174, v174, s28, v3
	v_med3_f32 v175, v175, s28, v3
	v_med3_f32 v176, v176, s28, v3
	v_med3_f32 v177, v177, s28, v3
	v_med3_f32 v178, v178, s28, v3
	v_med3_f32 v179, v179, s28, v3
	v_med3_f32 v180, v180, s28, v3
	v_med3_f32 v181, v181, s28, v3
	v_med3_f32 v182, v182, s28, v3
	v_med3_f32 v183, v183, s28, v3
	v_med3_f32 v184, v184, s28, v3
	v_med3_f32 v185, v185, s28, v3
	v_med3_f32 v186, v186, s28, v3
	v_med3_f32 v187, v187, s28, v3
	v_med3_f32 v188, v188, s28, v3
	v_med3_f32 v189, v189, s28, v3
	v_med3_f32 v190, v190, s28, v3
	v_med3_f32 v191, v191, s28, v3
	v_med3_f32 v192, v192, s28, v3
	v_med3_f32 v193, v193, s28, v3
	v_med3_f32 v194, v194, s28, v3
	v_med3_f32 v195, v195, s28, v3
	v_med3_f32 v196, v196, s28, v3
	v_med3_f32 v197, v197, s28, v3
	v_med3_f32 v198, v198, s28, v3
	v_med3_f32 v199, v199, s28, v3
	v_mov_b32_e32 v10, 0
	v_mov_b32_e32 v11, 0
	v_mov_b32_e32 v12, 0
	v_mov_b32_e32 v13, 0
	v_cvt_pk_fp8_f32 v10, v222, v226
	v_cvt_pk_fp8_f32 v11, v238, v242
	v_cvt_pk_fp8_f32 v12, v168, v172
	v_cvt_pk_fp8_f32 v13, v184, v188
	v_cvt_pk_fp8_f32 v10, v230, v234 op_sel:[0,0,1]
	v_cvt_pk_fp8_f32 v11, v160, v164 op_sel:[0,0,1]
	v_cvt_pk_fp8_f32 v12, v176, v180 op_sel:[0,0,1]
	v_cvt_pk_fp8_f32 v13, v192, v196 op_sel:[0,0,1]
	s_nop 1
	global_store_dwordx4 v6, v[10:13], s[16:17] nt
	s_add_u32 s16, s16, s25
	s_addc_u32 s17, s17, 0
	v_mov_b32_e32 v14, 0
	v_mov_b32_e32 v15, 0
	v_mov_b32_e32 v16, 0
	v_mov_b32_e32 v17, 0
	v_cvt_pk_fp8_f32 v14, v223, v227
	v_cvt_pk_fp8_f32 v15, v239, v243
	v_cvt_pk_fp8_f32 v16, v169, v173
	v_cvt_pk_fp8_f32 v17, v185, v189
	v_cvt_pk_fp8_f32 v14, v231, v235 op_sel:[0,0,1]
	v_cvt_pk_fp8_f32 v15, v161, v165 op_sel:[0,0,1]
	v_cvt_pk_fp8_f32 v16, v177, v181 op_sel:[0,0,1]
	v_cvt_pk_fp8_f32 v17, v193, v197 op_sel:[0,0,1]
	s_nop 1
	global_store_dwordx4 v6, v[14:17], s[16:17] nt
	s_add_u32 s16, s16, s25
	s_addc_u32 s17, s17, 0
	v_mov_b32_e32 v248, 0
	v_mov_b32_e32 v249, 0
	v_mov_b32_e32 v250, 0
	v_mov_b32_e32 v251, 0
	v_cvt_pk_fp8_f32 v248, v224, v228
	v_cvt_pk_fp8_f32 v249, v240, v244
	v_cvt_pk_fp8_f32 v250, v170, v174
	v_cvt_pk_fp8_f32 v251, v186, v190
	v_cvt_pk_fp8_f32 v248, v232, v236 op_sel:[0,0,1]
	v_cvt_pk_fp8_f32 v249, v162, v166 op_sel:[0,0,1]
	v_cvt_pk_fp8_f32 v250, v178, v182 op_sel:[0,0,1]
	v_cvt_pk_fp8_f32 v251, v194, v198 op_sel:[0,0,1]
	s_nop 1
	global_store_dwordx4 v6, v[248:251], s[16:17] nt
	s_add_u32 s16, s16, s25
	s_addc_u32 s17, s17, 0
	v_mov_b32_e32 v252, 0
	v_mov_b32_e32 v253, 0
	v_mov_b32_e32 v254, 0
	v_mov_b32_e32 v255, 0
	v_cvt_pk_fp8_f32 v252, v225, v229
	v_cvt_pk_fp8_f32 v253, v241, v245
	v_cvt_pk_fp8_f32 v254, v171, v175
	v_cvt_pk_fp8_f32 v255, v187, v191
	v_cvt_pk_fp8_f32 v252, v233, v237 op_sel:[0,0,1]
	v_cvt_pk_fp8_f32 v253, v163, v167 op_sel:[0,0,1]
	v_cvt_pk_fp8_f32 v254, v179, v183 op_sel:[0,0,1]
	v_cvt_pk_fp8_f32 v255, v195, v199 op_sel:[0,0,1]
	s_nop 1
	global_store_dwordx4 v6, v[252:255], s[16:17] nt
	s_branch .Lsf14_loop
.Lsf14_done:
	ds_read_b128 v[160:163], v7 offset:0
	ds_read_b128 v[164:167], v7 offset:1024
	ds_read_b128 v[168:171], v7 offset:2048
	ds_read_b128 v[172:175], v7 offset:3072
	ds_read_b128 v[176:179], v7 offset:4096
	ds_read_b128 v[180:183], v7 offset:5120
	ds_read_b128 v[184:187], v7 offset:6144
	ds_read_b128 v[188:191], v7 offset:7168
	ds_read_b128 v[192:195], v7 offset:8192
	ds_read_b128 v[196:199], v7 offset:9216
.Lsf14_skip:
	s_waitcnt lgkmcnt(0)
	s_barrier
